# grid barrier spin loops keep two polls of the generation word in flight (wait for the older one only) (on top of v27)
# speedup vs baseline: 1.0088x; 1.0088x over previous
.LBB0_294:
	v_readlane_b32 s14, v254, 41
	v_readlane_b32 s15, v254, 42
	s_add_i32 s29, s29, 1
	s_mov_b64 s[42:43], -1
	s_nop 2
	global_load_dword v2, v195, s[14:15] sc1
	s_waitcnt vmcnt(1)
	v_cmp_ne_u32_e32 vcc, v2, v3
	s_orn2_b64 s[40:41], vcc, exec
	s_branch .LBB0_291
.LBB0_295:
	v_readlane_b32 s14, v254, 5
	v_readlane_b32 s15, v254, 6
	s_nop 4
	global_load_dword v11, v195, s[14:15] sc1
	s_waitcnt vmcnt(0)
	v_cmp_eq_u32_e32 vcc, 0, v11
	s_cbranch_vccnz .LBB0_297
	s_mov_b64 s[42:43], -1
	s_branch .LBB0_291

.LBB0_305:
	s_or_b64 exec, exec, s[30:31]
	s_waitcnt vmcnt(0)
	v_readfirstlane_b32 s14, v4
	v_cvt_f32_u32_e32 v4, v2
	v_sub_u32_e32 v5, 0, v2
	v_add_u32_e32 v3, s14, v3
	v_readlane_b32 s14, v254, 45
	v_rcp_iflag_f32_e32 v4, v4
	v_readlane_b32 s15, v254, 46
	s_mov_b64 s[34:35], -1
	v_mul_f32_e32 v4, 0x4f7ffffe, v4
	v_cvt_u32_f32_e32 v4, v4
	v_mul_lo_u32 v5, v5, v4
	v_mul_hi_u32 v5, v4, v5
	v_add_u32_e32 v4, v4, v5
	v_mul_hi_u32 v4, v3, v4
	v_mul_lo_u32 v5, v4, v2
	v_sub_u32_e32 v5, v3, v5
	v_cmp_ge_u32_e32 vcc, v5, v2
	v_add_u32_e32 v6, 1, v4
	v_add_u32_e32 v3, 1, v3
	v_cndmask_b32_e32 v4, v4, v6, vcc
	v_sub_u32_e32 v6, v5, v2
	v_cndmask_b32_e32 v5, v5, v6, vcc
	v_cmp_ge_u32_e32 vcc, v5, v2
	v_add_u32_e32 v5, 1, v4
	s_nop 0
	v_cndmask_b32_e32 v4, v4, v5, vcc
	v_mul_lo_u32 v5, v2, v4
	v_add_u32_e32 v2, v5, v2
	v_cmp_ne_u32_e32 vcc, v3, v2
	v_mov_b64_e32 v[2:3], s[14:15]
	s_and_saveexec_b64 s[30:31], vcc
	s_cbranch_execz .LBB0_317
	v_readlane_b32 s14, v254, 45
	v_readlane_b32 s15, v254, 46
	s_nop 4
	global_load_dword v2, v195, s[14:15] sc1
	s_mov_b64 s[14:15], 0
	s_waitcnt vmcnt(0)
	v_cmp_eq_u32_e32 vcc, v2, v4
	s_and_saveexec_b64 s[34:35], vcc
	s_cbranch_execz .LBB0_316
	s_mov_b32 s29, 1
	v_mov_b32_e32 v10, v4
	s_mov_b64 s[36:37], 0
	s_branch .LBB0_309

.LBB0_311:
	v_readlane_b32 s14, v254, 45
	v_readlane_b32 s15, v254, 46
	s_add_i32 s29, s29, 1
	s_mov_b64 s[42:43], -1
	s_nop 2
	global_load_dword v10, v195, s[14:15] sc1
	s_waitcnt vmcnt(1)
	v_cmp_ne_u32_e32 vcc, v10, v4
	s_orn2_b64 s[40:41], vcc, exec
	s_branch .LBB0_308
